# in_proj sigmoid epilogues: 2^-5 accumulator scale folded into the -log2e constant (exact), on top of the gate_up epilogue rewrite
# speedup vs baseline: 1.0308x; 1.0024x over previous
.LBB0_549:
	s_mov_b32 s1, -1
	s_cmp_gt_i32 s0, 1
	v_mbcnt_lo_u32_b32 v0, s1, 0
	v_mbcnt_hi_u32_b32 v0, s1, v0
	v_and_b32_e32 v172, 15, v0
	v_bfe_u32 v134, v0, 4, 2
	s_mov_b64 s[22:23], -1
	v_mov_b32_e32 v240, v184
	s_cbranch_scc0 .LBB0_556
	s_cmp_gt_u32 s0, 3
	s_cbranch_scc0 .LBB0_552
	s_mov_b64 s[22:23], s[96:97]
	s_load_dwordx2 s[22:23], s[22:23], 0xe8
	s_lshl_b32 s1, s20, 8
	s_add_i32 s1, s1, s46
	v_or_b32_e32 v130, s1, v172
	v_ashrrev_i32_e32 v131, 31, v130
	v_lshlrev_b64 v[132:133], 11, v[130:131]
	s_waitcnt lgkmcnt(0)
	v_lshl_add_u64 v[132:133], s[22:23], 0, v[132:133]
	s_mov_b64 s[24:25], 0xbcaffc00
	v_mul_f32_e32 v131, 0xbd38aa3b, v126
	v_lshl_add_u64 v[136:137], v[132:133], 0, s[24:25]
	v_exp_f32_e32 v131, v131
	v_mul_f32_e32 v138, 0xbd38aa3b, v127
	v_exp_f32_e32 v138, v138
	v_mul_f32_e32 v132, 0xbd38aa3b, v128
	v_exp_f32_e32 v132, v132
	v_mul_f32_e32 v133, 0xbd38aa3b, v129
	v_mul_f32_e32 v135, 0xbd38aa3b, v122
	v_exp_f32_e32 v133, v133
	v_exp_f32_e32 v135, v135
	v_add_f32_e32 v131, 1.0, v131
	v_mul_f32_e32 v139, 0xbd38aa3b, v123
	v_rcp_f32_e32 v131, v131
	v_exp_f32_e32 v139, v139
	v_add_f32_e32 v138, 1.0, v138
	v_mul_f32_e32 v140, 0xbd38aa3b, v124
	v_rcp_f32_e32 v138, v138
	v_exp_f32_e32 v140, v140
	v_add_f32_e32 v132, 1.0, v132
	v_mul_f32_e32 v141, 0xbd38aa3b, v125
	v_rcp_f32_e32 v132, v132
	v_exp_f32_e32 v141, v141
	v_add_f32_e32 v133, 1.0, v133
	v_add_f32_e32 v135, 1.0, v135
	v_rcp_f32_e32 v133, v133
	v_rcp_f32_e32 v135, v135
	v_add_f32_e32 v139, 1.0, v139
	v_fma_f32 v131, v131, s87, -0.5
	v_rcp_f32_e32 v139, v139
	v_add_f32_e32 v140, 1.0, v140
	v_cvt_pk_u8_f32 v131, v131, 0, 0
	v_fma_f32 v138, v138, s87, -0.5
	v_rcp_f32_e32 v140, v140
	v_add_f32_e32 v141, 1.0, v141
	v_cvt_pk_u8_f32 v131, v138, 1, v131
	v_fma_f32 v132, v132, s87, -0.5
	v_rcp_f32_e32 v141, v141
	v_cvt_pk_u8_f32 v131, v132, 2, v131
	v_fma_f32 v132, v133, s87, -0.5
	v_cvt_pk_u8_f32 v132, v132, 3, v131
	v_fma_f32 v131, v135, s87, -0.5
	s_lshl_b32 s1, s0, 8
	v_cvt_pk_u8_f32 v131, v131, 0, 0
	v_fma_f32 v133, v139, s87, -0.5
	v_lshl_or_b32 v0, v134, 3, s1
	v_cvt_pk_u8_f32 v131, v133, 1, v131
	v_fma_f32 v133, v140, s87, -0.5
	v_or_b32_e32 v0, s47, v0
	v_cvt_pk_u8_f32 v131, v133, 2, v131
	v_fma_f32 v133, v141, s87, -0.5
	v_cvt_pk_u8_f32 v133, v133, 3, v131
	v_lshl_add_u64 v[138:139], v[136:137], 0, v[0:1]
	global_store_dwordx2 v[138:139], v[132:133], off
	v_mul_f32_e32 v131, 0xbd38aa3b, v118
	v_exp_f32_e32 v131, v131
	v_mul_f32_e32 v138, 0xbd38aa3b, v119
	v_exp_f32_e32 v138, v138
	v_mul_f32_e32 v132, 0xbd38aa3b, v120
	v_exp_f32_e32 v132, v132
	v_mul_f32_e32 v133, 0xbd38aa3b, v121
	v_mul_f32_e32 v135, 0xbd38aa3b, v114
	v_exp_f32_e32 v133, v133
	v_exp_f32_e32 v135, v135
	v_add_f32_e32 v131, 1.0, v131
	v_mul_f32_e32 v139, 0xbd38aa3b, v115
	v_rcp_f32_e32 v131, v131
	v_exp_f32_e32 v139, v139
	v_add_f32_e32 v138, 1.0, v138
	v_mul_f32_e32 v140, 0xbd38aa3b, v116
	v_rcp_f32_e32 v138, v138
	v_exp_f32_e32 v140, v140
	v_add_f32_e32 v132, 1.0, v132
	v_mul_f32_e32 v141, 0xbd38aa3b, v117
	v_rcp_f32_e32 v132, v132
	v_exp_f32_e32 v141, v141
	v_add_f32_e32 v133, 1.0, v133
	v_add_f32_e32 v135, 1.0, v135
	v_rcp_f32_e32 v133, v133
	v_rcp_f32_e32 v135, v135
	v_add_f32_e32 v139, 1.0, v139
	v_fma_f32 v131, v131, s87, -0.5
	v_rcp_f32_e32 v139, v139
	v_add_f32_e32 v140, 1.0, v140
	v_cvt_pk_u8_f32 v131, v131, 0, 0
	v_fma_f32 v138, v138, s87, -0.5
	v_rcp_f32_e32 v140, v140
	v_add_f32_e32 v141, 1.0, v141
	v_cvt_pk_u8_f32 v131, v138, 1, v131
	v_fma_f32 v132, v132, s87, -0.5
	v_rcp_f32_e32 v141, v141
	v_cvt_pk_u8_f32 v131, v132, 2, v131
	v_fma_f32 v132, v133, s87, -0.5
	v_cvt_pk_u8_f32 v138, v132, 3, v131
	v_fma_f32 v131, v135, s87, -0.5
	v_cvt_pk_u8_f32 v131, v131, 0, 0
	v_fma_f32 v132, v139, s87, -0.5
	v_cvt_pk_u8_f32 v131, v132, 1, v131
	v_fma_f32 v132, v140, s87, -0.5
	v_cvt_pk_u8_f32 v131, v132, 2, v131
	v_fma_f32 v132, v141, s87, -0.5
	v_cvt_pk_u8_f32 v139, v132, 3, v131
	v_or_b32_e32 v132, 0x80, v0
	v_mov_b32_e32 v133, v1
	v_lshl_add_u64 v[136:137], v[136:137], 0, v[132:133]
	v_mul_f32_e32 v131, 0xbd38aa3b, v110
	global_store_dwordx2 v[136:137], v[138:139], off
	v_exp_f32_e32 v131, v131
	v_mul_f32_e32 v140, 0xbd38aa3b, v111
	v_exp_f32_e32 v140, v140
	v_mul_f32_e32 v138, 0xbd38aa3b, v112
	v_exp_f32_e32 v138, v138
	v_mul_f32_e32 v139, 0xbd38aa3b, v113
	v_mul_f32_e32 v135, 0xbd38aa3b, v106
	v_exp_f32_e32 v139, v139
	v_exp_f32_e32 v135, v135
	v_add_f32_e32 v131, 1.0, v131
	v_mul_f32_e32 v141, 0xbd38aa3b, v107
	v_rcp_f32_e32 v131, v131
	v_exp_f32_e32 v141, v141
	v_add_f32_e32 v140, 1.0, v140
	v_mul_f32_e32 v142, 0xbd38aa3b, v108
	v_rcp_f32_e32 v140, v140
	v_exp_f32_e32 v142, v142
	v_add_f32_e32 v138, 1.0, v138
	v_mul_f32_e32 v143, 0xbd38aa3b, v109
	v_rcp_f32_e32 v138, v138
	v_exp_f32_e32 v143, v143
	v_add_f32_e32 v139, 1.0, v139
	v_add_f32_e32 v135, 1.0, v135
	v_rcp_f32_e32 v139, v139
	v_rcp_f32_e32 v135, v135
	v_add_f32_e32 v141, 1.0, v141
	v_fma_f32 v131, v131, s87, -0.5
	v_rcp_f32_e32 v141, v141
	v_add_f32_e32 v142, 1.0, v142
	v_cvt_pk_u8_f32 v131, v131, 0, 0
	v_fma_f32 v140, v140, s87, -0.5
	v_rcp_f32_e32 v142, v142
	v_add_f32_e32 v143, 1.0, v143
	v_cvt_pk_u8_f32 v131, v140, 1, v131
	v_fma_f32 v138, v138, s87, -0.5
	v_or_b32_e32 v136, 16, v130
	v_rcp_f32_e32 v143, v143
	v_cvt_pk_u8_f32 v131, v138, 2, v131
	v_fma_f32 v138, v139, s87, -0.5
	v_ashrrev_i32_e32 v137, 31, v136
	v_cvt_pk_u8_f32 v138, v138, 3, v131
	v_fma_f32 v131, v135, s87, -0.5
	v_lshlrev_b64 v[136:137], 11, v[136:137]
	v_cvt_pk_u8_f32 v131, v131, 0, 0
	v_fma_f32 v135, v141, s87, -0.5
	v_lshl_add_u64 v[136:137], s[22:23], 0, v[136:137]
	v_cvt_pk_u8_f32 v131, v135, 1, v131
	v_fma_f32 v135, v142, s87, -0.5
	v_lshl_add_u64 v[136:137], v[136:137], 0, s[24:25]
	v_cvt_pk_u8_f32 v131, v135, 2, v131
	v_fma_f32 v135, v143, s87, -0.5
	v_cvt_pk_u8_f32 v139, v135, 3, v131
	v_lshl_add_u64 v[140:141], v[136:137], 0, v[0:1]
	global_store_dwordx2 v[140:141], v[138:139], off
	v_mul_f32_e32 v131, 0xbd38aa3b, v102
	v_exp_f32_e32 v131, v131
	v_mul_f32_e32 v140, 0xbd38aa3b, v103
	v_exp_f32_e32 v140, v140
	v_mul_f32_e32 v138, 0xbd38aa3b, v104
	v_exp_f32_e32 v138, v138
	v_mul_f32_e32 v139, 0xbd38aa3b, v105
	v_mul_f32_e32 v135, 0xbd38aa3b, v94
	v_exp_f32_e32 v139, v139
	v_exp_f32_e32 v135, v135
	v_add_f32_e32 v131, 1.0, v131
	v_mul_f32_e32 v141, 0xbd38aa3b, v95
	v_rcp_f32_e32 v131, v131
	v_exp_f32_e32 v141, v141
	v_add_f32_e32 v140, 1.0, v140
	v_mul_f32_e32 v142, 0xbd38aa3b, v96
	v_rcp_f32_e32 v140, v140
	v_exp_f32_e32 v142, v142
	v_add_f32_e32 v138, 1.0, v138
	v_mul_f32_e32 v143, 0xbd38aa3b, v97
	v_rcp_f32_e32 v138, v138
	v_exp_f32_e32 v143, v143
	v_add_f32_e32 v139, 1.0, v139
	v_add_f32_e32 v135, 1.0, v135
	v_rcp_f32_e32 v139, v139
	v_rcp_f32_e32 v135, v135
	v_add_f32_e32 v141, 1.0, v141
	v_fma_f32 v131, v131, s87, -0.5
	v_rcp_f32_e32 v141, v141
	v_add_f32_e32 v142, 1.0, v142
	v_cvt_pk_u8_f32 v131, v131, 0, 0
	v_fma_f32 v140, v140, s87, -0.5
	v_rcp_f32_e32 v142, v142
	v_add_f32_e32 v143, 1.0, v143
	v_cvt_pk_u8_f32 v131, v140, 1, v131
	v_fma_f32 v138, v138, s87, -0.5
	v_rcp_f32_e32 v143, v143
	v_cvt_pk_u8_f32 v131, v138, 2, v131
	v_fma_f32 v138, v139, s87, -0.5
	v_cvt_pk_u8_f32 v138, v138, 3, v131
	v_fma_f32 v131, v135, s87, -0.5
	v_cvt_pk_u8_f32 v131, v131, 0, 0
	v_fma_f32 v135, v141, s87, -0.5
	v_cvt_pk_u8_f32 v131, v135, 1, v131
	v_fma_f32 v135, v142, s87, -0.5
	v_cvt_pk_u8_f32 v131, v135, 2, v131
	v_fma_f32 v135, v143, s87, -0.5
	v_cvt_pk_u8_f32 v139, v135, 3, v131
	v_lshl_add_u64 v[136:137], v[136:137], 0, v[132:133]
	v_mul_f32_e32 v131, 0xbd38aa3b, v98
	global_store_dwordx2 v[136:137], v[138:139], off
	v_exp_f32_e32 v131, v131
	v_mul_f32_e32 v140, 0xbd38aa3b, v99
	v_exp_f32_e32 v140, v140
	v_mul_f32_e32 v138, 0xbd38aa3b, v100
	v_exp_f32_e32 v138, v138
	v_mul_f32_e32 v139, 0xbd38aa3b, v101
	v_mul_f32_e32 v135, 0xbd38aa3b, v90
	v_exp_f32_e32 v139, v139
	v_exp_f32_e32 v135, v135
	v_add_f32_e32 v131, 1.0, v131
	v_mul_f32_e32 v141, 0xbd38aa3b, v91
	v_rcp_f32_e32 v131, v131
	v_exp_f32_e32 v141, v141
	v_add_f32_e32 v140, 1.0, v140
	v_mul_f32_e32 v142, 0xbd38aa3b, v92
	v_rcp_f32_e32 v140, v140
	v_exp_f32_e32 v142, v142
	v_add_f32_e32 v138, 1.0, v138
	v_mul_f32_e32 v143, 0xbd38aa3b, v93
	v_rcp_f32_e32 v138, v138
	v_exp_f32_e32 v143, v143
	v_add_f32_e32 v139, 1.0, v139
	v_add_f32_e32 v135, 1.0, v135
	v_rcp_f32_e32 v139, v139
	v_rcp_f32_e32 v135, v135
	v_add_f32_e32 v141, 1.0, v141
	v_fma_f32 v131, v131, s87, -0.5
	v_rcp_f32_e32 v141, v141
	v_add_f32_e32 v142, 1.0, v142
	v_cvt_pk_u8_f32 v131, v131, 0, 0
	v_fma_f32 v140, v140, s87, -0.5
	v_rcp_f32_e32 v142, v142
	v_add_f32_e32 v143, 1.0, v143
	v_cvt_pk_u8_f32 v131, v140, 1, v131
	v_fma_f32 v138, v138, s87, -0.5
	v_or_b32_e32 v136, 32, v130
	v_rcp_f32_e32 v143, v143
	v_cvt_pk_u8_f32 v131, v138, 2, v131
	v_fma_f32 v138, v139, s87, -0.5
	v_ashrrev_i32_e32 v137, 31, v136
	v_cvt_pk_u8_f32 v138, v138, 3, v131
	v_fma_f32 v131, v135, s87, -0.5
	v_lshlrev_b64 v[136:137], 11, v[136:137]
	v_cvt_pk_u8_f32 v131, v131, 0, 0
	v_fma_f32 v135, v141, s87, -0.5
	v_lshl_add_u64 v[136:137], s[22:23], 0, v[136:137]
	v_cvt_pk_u8_f32 v131, v135, 1, v131
	v_fma_f32 v135, v142, s87, -0.5
	v_lshl_add_u64 v[136:137], v[136:137], 0, s[24:25]
	v_cvt_pk_u8_f32 v131, v135, 2, v131
	v_fma_f32 v135, v143, s87, -0.5
	v_cvt_pk_u8_f32 v139, v135, 3, v131
	v_lshl_add_u64 v[140:141], v[136:137], 0, v[0:1]
	global_store_dwordx2 v[140:141], v[138:139], off
	v_mul_f32_e32 v131, 0xbd38aa3b, v86
	v_exp_f32_e32 v131, v131
	v_mul_f32_e32 v140, 0xbd38aa3b, v87
	v_exp_f32_e32 v140, v140
	v_mul_f32_e32 v138, 0xbd38aa3b, v88
	v_exp_f32_e32 v138, v138
	v_mul_f32_e32 v139, 0xbd38aa3b, v89
	v_mul_f32_e32 v135, 0xbd38aa3b, v78
	v_exp_f32_e32 v139, v139
	v_exp_f32_e32 v135, v135
	v_add_f32_e32 v131, 1.0, v131
	v_mul_f32_e32 v141, 0xbd38aa3b, v79
	v_rcp_f32_e32 v131, v131
	v_exp_f32_e32 v141, v141
	v_add_f32_e32 v140, 1.0, v140
	v_mul_f32_e32 v142, 0xbd38aa3b, v80
	v_rcp_f32_e32 v140, v140
	v_exp_f32_e32 v142, v142
	v_add_f32_e32 v138, 1.0, v138
	v_mul_f32_e32 v143, 0xbd38aa3b, v81
	v_rcp_f32_e32 v138, v138
	v_exp_f32_e32 v143, v143
	v_add_f32_e32 v139, 1.0, v139
	v_add_f32_e32 v135, 1.0, v135
	v_rcp_f32_e32 v139, v139
	v_rcp_f32_e32 v135, v135
	v_add_f32_e32 v141, 1.0, v141
	v_fma_f32 v131, v131, s87, -0.5
	v_rcp_f32_e32 v141, v141
	v_add_f32_e32 v142, 1.0, v142
	v_cvt_pk_u8_f32 v131, v131, 0, 0
	v_fma_f32 v140, v140, s87, -0.5
	v_rcp_f32_e32 v142, v142
	v_add_f32_e32 v143, 1.0, v143
	v_cvt_pk_u8_f32 v131, v140, 1, v131
	v_fma_f32 v138, v138, s87, -0.5
	v_rcp_f32_e32 v143, v143
	v_cvt_pk_u8_f32 v131, v138, 2, v131
	v_fma_f32 v138, v139, s87, -0.5
	v_cvt_pk_u8_f32 v138, v138, 3, v131
	v_fma_f32 v131, v135, s87, -0.5
	v_cvt_pk_u8_f32 v131, v131, 0, 0
	v_fma_f32 v135, v141, s87, -0.5
	v_cvt_pk_u8_f32 v131, v135, 1, v131
	v_fma_f32 v135, v142, s87, -0.5
	v_cvt_pk_u8_f32 v131, v135, 2, v131
	v_fma_f32 v135, v143, s87, -0.5
	v_cvt_pk_u8_f32 v139, v135, 3, v131
	v_lshl_add_u64 v[136:137], v[136:137], 0, v[132:133]
	v_mul_f32_e32 v131, 0xbd38aa3b, v82
	global_store_dwordx2 v[136:137], v[138:139], off
	v_exp_f32_e32 v131, v131
	v_mul_f32_e32 v140, 0xbd38aa3b, v83
	v_exp_f32_e32 v140, v140
	v_mul_f32_e32 v138, 0xbd38aa3b, v84
	v_exp_f32_e32 v138, v138
	v_mul_f32_e32 v139, 0xbd38aa3b, v85
	v_mul_f32_e32 v135, 0xbd38aa3b, v74
	v_exp_f32_e32 v139, v139
	v_exp_f32_e32 v135, v135
	v_add_f32_e32 v131, 1.0, v131
	v_mul_f32_e32 v141, 0xbd38aa3b, v75
	v_rcp_f32_e32 v131, v131
	v_exp_f32_e32 v141, v141
	v_add_f32_e32 v140, 1.0, v140
	v_mul_f32_e32 v142, 0xbd38aa3b, v76
	v_rcp_f32_e32 v140, v140
	v_exp_f32_e32 v142, v142
	v_add_f32_e32 v138, 1.0, v138
	v_mul_f32_e32 v143, 0xbd38aa3b, v77
	v_rcp_f32_e32 v138, v138
	v_exp_f32_e32 v143, v143
	v_add_f32_e32 v139, 1.0, v139
	v_add_f32_e32 v135, 1.0, v135
	v_rcp_f32_e32 v139, v139
	v_rcp_f32_e32 v135, v135
	v_add_f32_e32 v141, 1.0, v141
	v_fma_f32 v131, v131, s87, -0.5
	v_rcp_f32_e32 v141, v141
	v_add_f32_e32 v142, 1.0, v142
	v_cvt_pk_u8_f32 v131, v131, 0, 0
	v_fma_f32 v140, v140, s87, -0.5
	v_rcp_f32_e32 v142, v142
	v_add_f32_e32 v143, 1.0, v143
	v_cvt_pk_u8_f32 v131, v140, 1, v131
	v_fma_f32 v138, v138, s87, -0.5
	v_or_b32_e32 v136, 48, v130
	v_rcp_f32_e32 v143, v143
	v_cvt_pk_u8_f32 v131, v138, 2, v131
	v_fma_f32 v138, v139, s87, -0.5
	v_ashrrev_i32_e32 v137, 31, v136
	v_cvt_pk_u8_f32 v138, v138, 3, v131
	v_fma_f32 v131, v135, s87, -0.5
	v_lshlrev_b64 v[136:137], 11, v[136:137]
	v_cvt_pk_u8_f32 v131, v131, 0, 0
	v_fma_f32 v135, v141, s87, -0.5
	v_lshl_add_u64 v[136:137], s[22:23], 0, v[136:137]
	v_cvt_pk_u8_f32 v131, v135, 1, v131
	v_fma_f32 v135, v142, s87, -0.5
	v_lshl_add_u64 v[136:137], v[136:137], 0, s[24:25]
	v_cvt_pk_u8_f32 v131, v135, 2, v131
	v_fma_f32 v135, v143, s87, -0.5
	v_cvt_pk_u8_f32 v139, v135, 3, v131
	v_lshl_add_u64 v[140:141], v[136:137], 0, v[0:1]
	global_store_dwordx2 v[140:141], v[138:139], off
	v_mul_f32_e32 v131, 0xbd38aa3b, v70
	v_exp_f32_e32 v131, v131
	v_mul_f32_e32 v140, 0xbd38aa3b, v71
	v_exp_f32_e32 v140, v140
	v_mul_f32_e32 v138, 0xbd38aa3b, v72
	v_exp_f32_e32 v138, v138
	v_mul_f32_e32 v139, 0xbd38aa3b, v73
	v_mul_f32_e32 v135, 0xbd38aa3b, v66
	v_exp_f32_e32 v139, v139
	v_exp_f32_e32 v135, v135
	v_add_f32_e32 v131, 1.0, v131
	v_mul_f32_e32 v141, 0xbd38aa3b, v67
	v_rcp_f32_e32 v131, v131
	v_exp_f32_e32 v141, v141
	v_add_f32_e32 v140, 1.0, v140
	v_mul_f32_e32 v142, 0xbd38aa3b, v68
	v_rcp_f32_e32 v140, v140
	v_exp_f32_e32 v142, v142
	v_add_f32_e32 v138, 1.0, v138
	v_mul_f32_e32 v143, 0xbd38aa3b, v69
	v_rcp_f32_e32 v138, v138
	v_exp_f32_e32 v143, v143
	v_add_f32_e32 v139, 1.0, v139
	v_add_f32_e32 v135, 1.0, v135
	v_rcp_f32_e32 v139, v139
	v_rcp_f32_e32 v135, v135
	v_add_f32_e32 v141, 1.0, v141
	v_fma_f32 v131, v131, s87, -0.5
	v_rcp_f32_e32 v141, v141
	v_add_f32_e32 v142, 1.0, v142
	v_cvt_pk_u8_f32 v131, v131, 0, 0
	v_fma_f32 v140, v140, s87, -0.5
	v_rcp_f32_e32 v142, v142
	v_add_f32_e32 v143, 1.0, v143
	v_cvt_pk_u8_f32 v131, v140, 1, v131
	v_fma_f32 v138, v138, s87, -0.5
	v_rcp_f32_e32 v143, v143
	v_cvt_pk_u8_f32 v131, v138, 2, v131
	v_fma_f32 v138, v139, s87, -0.5
	v_cvt_pk_u8_f32 v138, v138, 3, v131
	v_fma_f32 v131, v135, s87, -0.5
	v_cvt_pk_u8_f32 v131, v131, 0, 0
	v_fma_f32 v135, v141, s87, -0.5
	v_cvt_pk_u8_f32 v131, v135, 1, v131
	v_fma_f32 v135, v142, s87, -0.5
	v_cvt_pk_u8_f32 v131, v135, 2, v131
	v_fma_f32 v135, v143, s87, -0.5
	v_cvt_pk_u8_f32 v139, v135, 3, v131
	v_lshl_add_u64 v[136:137], v[136:137], 0, v[132:133]
	v_mul_f32_e32 v131, 0xbd38aa3b, v62
	global_store_dwordx2 v[136:137], v[138:139], off
	v_exp_f32_e32 v131, v131
	v_mul_f32_e32 v140, 0xbd38aa3b, v63
	v_exp_f32_e32 v140, v140
	v_mul_f32_e32 v138, 0xbd38aa3b, v64
	v_exp_f32_e32 v138, v138
	v_mul_f32_e32 v139, 0xbd38aa3b, v65
	v_mul_f32_e32 v135, 0xbd38aa3b, v58
	v_exp_f32_e32 v139, v139
	v_exp_f32_e32 v135, v135
	v_add_f32_e32 v131, 1.0, v131
	v_mul_f32_e32 v141, 0xbd38aa3b, v59
	v_rcp_f32_e32 v131, v131
	v_exp_f32_e32 v141, v141
	v_add_f32_e32 v140, 1.0, v140
	v_mul_f32_e32 v142, 0xbd38aa3b, v60
	v_rcp_f32_e32 v140, v140
	v_exp_f32_e32 v142, v142
	v_add_f32_e32 v138, 1.0, v138
	v_mul_f32_e32 v143, 0xbd38aa3b, v61
	v_rcp_f32_e32 v138, v138
	v_exp_f32_e32 v143, v143
	v_add_f32_e32 v139, 1.0, v139
	v_add_f32_e32 v135, 1.0, v135
	v_rcp_f32_e32 v139, v139
	v_rcp_f32_e32 v135, v135
	v_add_f32_e32 v141, 1.0, v141
	v_fma_f32 v131, v131, s87, -0.5
	v_rcp_f32_e32 v141, v141
	v_add_f32_e32 v142, 1.0, v142
	v_cvt_pk_u8_f32 v131, v131, 0, 0
	v_fma_f32 v140, v140, s87, -0.5
	v_rcp_f32_e32 v142, v142
	v_add_f32_e32 v143, 1.0, v143
	v_cvt_pk_u8_f32 v131, v140, 1, v131
	v_fma_f32 v138, v138, s87, -0.5
	v_add_u32_e32 v136, 0x80, v130
	v_rcp_f32_e32 v143, v143
	v_cvt_pk_u8_f32 v131, v138, 2, v131
	v_fma_f32 v138, v139, s87, -0.5
	v_ashrrev_i32_e32 v137, 31, v136
	v_cvt_pk_u8_f32 v138, v138, 3, v131
	v_fma_f32 v131, v135, s87, -0.5
	v_lshlrev_b64 v[136:137], 11, v[136:137]
	v_cvt_pk_u8_f32 v131, v131, 0, 0
	v_fma_f32 v135, v141, s87, -0.5
	v_lshl_add_u64 v[136:137], s[22:23], 0, v[136:137]
	v_cvt_pk_u8_f32 v131, v135, 1, v131
	v_fma_f32 v135, v142, s87, -0.5
	v_lshl_add_u64 v[136:137], v[136:137], 0, s[24:25]
	v_cvt_pk_u8_f32 v131, v135, 2, v131
	v_fma_f32 v135, v143, s87, -0.5
	v_cvt_pk_u8_f32 v139, v135, 3, v131
	v_lshl_add_u64 v[140:141], v[136:137], 0, v[0:1]
	global_store_dwordx2 v[140:141], v[138:139], off
	v_mul_f32_e32 v131, 0xbd38aa3b, v54
	v_exp_f32_e32 v131, v131
	v_mul_f32_e32 v140, 0xbd38aa3b, v55
	v_exp_f32_e32 v140, v140
	v_mul_f32_e32 v138, 0xbd38aa3b, v56
	v_exp_f32_e32 v138, v138
	v_mul_f32_e32 v139, 0xbd38aa3b, v57
	v_mul_f32_e32 v135, 0xbd38aa3b, v46
	v_exp_f32_e32 v139, v139
	v_exp_f32_e32 v135, v135
	v_add_f32_e32 v131, 1.0, v131
	v_mul_f32_e32 v141, 0xbd38aa3b, v47
	v_rcp_f32_e32 v131, v131
	v_exp_f32_e32 v141, v141
	v_add_f32_e32 v140, 1.0, v140
	v_mul_f32_e32 v142, 0xbd38aa3b, v48
	v_rcp_f32_e32 v140, v140
	v_exp_f32_e32 v142, v142
	v_add_f32_e32 v138, 1.0, v138
	v_mul_f32_e32 v143, 0xbd38aa3b, v49
	v_rcp_f32_e32 v138, v138
	v_exp_f32_e32 v143, v143
	v_add_f32_e32 v139, 1.0, v139
	v_add_f32_e32 v135, 1.0, v135
	v_rcp_f32_e32 v139, v139
	v_rcp_f32_e32 v135, v135
	v_add_f32_e32 v141, 1.0, v141
	v_fma_f32 v131, v131, s87, -0.5
	v_rcp_f32_e32 v141, v141
	v_add_f32_e32 v142, 1.0, v142
	v_cvt_pk_u8_f32 v131, v131, 0, 0
	v_fma_f32 v140, v140, s87, -0.5
	v_rcp_f32_e32 v142, v142
	v_add_f32_e32 v143, 1.0, v143
	v_cvt_pk_u8_f32 v131, v140, 1, v131
	v_fma_f32 v138, v138, s87, -0.5
	v_rcp_f32_e32 v143, v143
	v_cvt_pk_u8_f32 v131, v138, 2, v131
	v_fma_f32 v138, v139, s87, -0.5
	v_cvt_pk_u8_f32 v138, v138, 3, v131
	v_fma_f32 v131, v135, s87, -0.5
	v_cvt_pk_u8_f32 v131, v131, 0, 0
	v_fma_f32 v135, v141, s87, -0.5
	v_cvt_pk_u8_f32 v131, v135, 1, v131
	v_fma_f32 v135, v142, s87, -0.5
	v_cvt_pk_u8_f32 v131, v135, 2, v131
	v_fma_f32 v135, v143, s87, -0.5
	v_cvt_pk_u8_f32 v139, v135, 3, v131
	v_lshl_add_u64 v[136:137], v[136:137], 0, v[132:133]
	v_mul_f32_e32 v131, 0xbd38aa3b, v50
	global_store_dwordx2 v[136:137], v[138:139], off
	v_exp_f32_e32 v131, v131
	v_mul_f32_e32 v140, 0xbd38aa3b, v51
	v_exp_f32_e32 v140, v140
	v_mul_f32_e32 v138, 0xbd38aa3b, v52
	v_exp_f32_e32 v138, v138
	v_mul_f32_e32 v139, 0xbd38aa3b, v53
	v_mul_f32_e32 v135, 0xbd38aa3b, v42
	v_exp_f32_e32 v139, v139
	v_exp_f32_e32 v135, v135
	v_add_f32_e32 v131, 1.0, v131
	v_mul_f32_e32 v141, 0xbd38aa3b, v43
	v_rcp_f32_e32 v131, v131
	v_exp_f32_e32 v141, v141
	v_add_f32_e32 v140, 1.0, v140
	v_mul_f32_e32 v142, 0xbd38aa3b, v44
	v_rcp_f32_e32 v140, v140
	v_exp_f32_e32 v142, v142
	v_add_f32_e32 v138, 1.0, v138
	v_mul_f32_e32 v143, 0xbd38aa3b, v45
	v_rcp_f32_e32 v138, v138
	v_exp_f32_e32 v143, v143
	v_add_f32_e32 v139, 1.0, v139
	v_add_f32_e32 v135, 1.0, v135
	v_rcp_f32_e32 v139, v139
	v_rcp_f32_e32 v135, v135
	v_add_f32_e32 v141, 1.0, v141
	v_fma_f32 v131, v131, s87, -0.5
	v_rcp_f32_e32 v141, v141
	v_add_f32_e32 v142, 1.0, v142
	v_cvt_pk_u8_f32 v131, v131, 0, 0
	v_fma_f32 v140, v140, s87, -0.5
	v_rcp_f32_e32 v142, v142
	v_add_f32_e32 v143, 1.0, v143
	v_cvt_pk_u8_f32 v131, v140, 1, v131
	v_fma_f32 v138, v138, s87, -0.5
	v_add_u32_e32 v136, 0x90, v130
	v_rcp_f32_e32 v143, v143
	v_cvt_pk_u8_f32 v131, v138, 2, v131
	v_fma_f32 v138, v139, s87, -0.5
	v_ashrrev_i32_e32 v137, 31, v136
	v_cvt_pk_u8_f32 v138, v138, 3, v131
	v_fma_f32 v131, v135, s87, -0.5
	v_lshlrev_b64 v[136:137], 11, v[136:137]
	v_cvt_pk_u8_f32 v131, v131, 0, 0
	v_fma_f32 v135, v141, s87, -0.5
	v_lshl_add_u64 v[136:137], s[22:23], 0, v[136:137]
	v_cvt_pk_u8_f32 v131, v135, 1, v131
	v_fma_f32 v135, v142, s87, -0.5
	v_lshl_add_u64 v[136:137], v[136:137], 0, s[24:25]
	v_cvt_pk_u8_f32 v131, v135, 2, v131
	v_fma_f32 v135, v143, s87, -0.5
	v_cvt_pk_u8_f32 v139, v135, 3, v131
	v_lshl_add_u64 v[140:141], v[136:137], 0, v[0:1]
	global_store_dwordx2 v[140:141], v[138:139], off
	v_mul_f32_e32 v131, 0xbd38aa3b, v38
	v_exp_f32_e32 v131, v131
	v_mul_f32_e32 v140, 0xbd38aa3b, v39
	v_exp_f32_e32 v140, v140
	v_mul_f32_e32 v138, 0xbd38aa3b, v40
	v_exp_f32_e32 v138, v138
	v_mul_f32_e32 v139, 0xbd38aa3b, v41
	v_mul_f32_e32 v135, 0xbd38aa3b, v30
	v_exp_f32_e32 v139, v139
	v_exp_f32_e32 v135, v135
	v_add_f32_e32 v131, 1.0, v131
	v_mul_f32_e32 v141, 0xbd38aa3b, v31
	v_rcp_f32_e32 v131, v131
	v_exp_f32_e32 v141, v141
	v_add_f32_e32 v140, 1.0, v140
	v_mul_f32_e32 v142, 0xbd38aa3b, v32
	v_rcp_f32_e32 v140, v140
	v_exp_f32_e32 v142, v142
	v_add_f32_e32 v138, 1.0, v138
	v_mul_f32_e32 v143, 0xbd38aa3b, v33
	v_rcp_f32_e32 v138, v138
	v_exp_f32_e32 v143, v143
	v_add_f32_e32 v139, 1.0, v139
	v_add_f32_e32 v135, 1.0, v135
	v_rcp_f32_e32 v139, v139
	v_rcp_f32_e32 v135, v135
	v_add_f32_e32 v141, 1.0, v141
	v_fma_f32 v131, v131, s87, -0.5
	v_rcp_f32_e32 v141, v141
	v_add_f32_e32 v142, 1.0, v142
	v_cvt_pk_u8_f32 v131, v131, 0, 0
	v_fma_f32 v140, v140, s87, -0.5
	v_rcp_f32_e32 v142, v142
	v_add_f32_e32 v143, 1.0, v143
	v_cvt_pk_u8_f32 v131, v140, 1, v131
	v_fma_f32 v138, v138, s87, -0.5
	v_rcp_f32_e32 v143, v143
	v_cvt_pk_u8_f32 v131, v138, 2, v131
	v_fma_f32 v138, v139, s87, -0.5
	v_cvt_pk_u8_f32 v138, v138, 3, v131
	v_fma_f32 v131, v135, s87, -0.5
	v_cvt_pk_u8_f32 v131, v131, 0, 0
	v_fma_f32 v135, v141, s87, -0.5
	v_cvt_pk_u8_f32 v131, v135, 1, v131
	v_fma_f32 v135, v142, s87, -0.5
	v_cvt_pk_u8_f32 v131, v135, 2, v131
	v_fma_f32 v135, v143, s87, -0.5
	v_cvt_pk_u8_f32 v139, v135, 3, v131
	v_lshl_add_u64 v[136:137], v[136:137], 0, v[132:133]
	v_mul_f32_e32 v131, 0xbd38aa3b, v34
	global_store_dwordx2 v[136:137], v[138:139], off
	v_exp_f32_e32 v131, v131
	v_mul_f32_e32 v140, 0xbd38aa3b, v35
	v_exp_f32_e32 v140, v140
	v_mul_f32_e32 v138, 0xbd38aa3b, v36
	v_exp_f32_e32 v138, v138
	v_mul_f32_e32 v139, 0xbd38aa3b, v37
	v_mul_f32_e32 v135, 0xbd38aa3b, v26
	v_exp_f32_e32 v139, v139
	v_exp_f32_e32 v135, v135
	v_add_f32_e32 v131, 1.0, v131
	v_mul_f32_e32 v141, 0xbd38aa3b, v27
	v_rcp_f32_e32 v131, v131
	v_exp_f32_e32 v141, v141
	v_add_f32_e32 v140, 1.0, v140
	v_mul_f32_e32 v142, 0xbd38aa3b, v28
	v_rcp_f32_e32 v140, v140
	v_exp_f32_e32 v142, v142
	v_add_f32_e32 v138, 1.0, v138
	v_mul_f32_e32 v143, 0xbd38aa3b, v29
	v_rcp_f32_e32 v138, v138
	v_exp_f32_e32 v143, v143
	v_add_f32_e32 v139, 1.0, v139
	v_add_f32_e32 v135, 1.0, v135
	v_rcp_f32_e32 v139, v139
	v_rcp_f32_e32 v135, v135
	v_add_f32_e32 v141, 1.0, v141
	v_fma_f32 v131, v131, s87, -0.5
	v_rcp_f32_e32 v141, v141
	v_add_f32_e32 v142, 1.0, v142
	v_cvt_pk_u8_f32 v131, v131, 0, 0
	v_fma_f32 v140, v140, s87, -0.5
	v_rcp_f32_e32 v142, v142
	v_add_f32_e32 v143, 1.0, v143
	v_cvt_pk_u8_f32 v131, v140, 1, v131
	v_fma_f32 v138, v138, s87, -0.5
	v_add_u32_e32 v136, 0xa0, v130
	v_rcp_f32_e32 v143, v143
	v_cvt_pk_u8_f32 v131, v138, 2, v131
	v_fma_f32 v138, v139, s87, -0.5
	v_ashrrev_i32_e32 v137, 31, v136
	v_cvt_pk_u8_f32 v138, v138, 3, v131
	v_fma_f32 v131, v135, s87, -0.5
	v_lshlrev_b64 v[136:137], 11, v[136:137]
	v_cvt_pk_u8_f32 v131, v131, 0, 0
	v_fma_f32 v135, v141, s87, -0.5
	v_lshl_add_u64 v[136:137], s[22:23], 0, v[136:137]
	v_cvt_pk_u8_f32 v131, v135, 1, v131
	v_fma_f32 v135, v142, s87, -0.5
	v_lshl_add_u64 v[136:137], v[136:137], 0, s[24:25]
	v_cvt_pk_u8_f32 v131, v135, 2, v131
	v_fma_f32 v135, v143, s87, -0.5
	v_cvt_pk_u8_f32 v139, v135, 3, v131
	v_lshl_add_u64 v[140:141], v[136:137], 0, v[0:1]
	global_store_dwordx2 v[140:141], v[138:139], off
	v_mul_f32_e32 v131, 0xbd38aa3b, v22
	v_exp_f32_e32 v131, v131
	v_mul_f32_e32 v140, 0xbd38aa3b, v23
	v_exp_f32_e32 v140, v140
	v_mul_f32_e32 v138, 0xbd38aa3b, v24
	v_exp_f32_e32 v138, v138
	v_mul_f32_e32 v139, 0xbd38aa3b, v25
	v_mul_f32_e32 v135, 0xbd38aa3b, v14
	v_exp_f32_e32 v139, v139
	v_exp_f32_e32 v135, v135
	v_add_f32_e32 v131, 1.0, v131
	v_mul_f32_e32 v141, 0xbd38aa3b, v15
	v_rcp_f32_e32 v131, v131
	v_exp_f32_e32 v141, v141
	v_add_f32_e32 v140, 1.0, v140
	v_mul_f32_e32 v142, 0xbd38aa3b, v16
	v_rcp_f32_e32 v140, v140
	v_exp_f32_e32 v142, v142
	v_add_f32_e32 v138, 1.0, v138
	v_mul_f32_e32 v143, 0xbd38aa3b, v17
	v_rcp_f32_e32 v138, v138
	v_exp_f32_e32 v143, v143
	v_add_f32_e32 v139, 1.0, v139
	v_add_f32_e32 v135, 1.0, v135
	v_rcp_f32_e32 v139, v139
	v_rcp_f32_e32 v135, v135
	v_add_f32_e32 v141, 1.0, v141
	v_fma_f32 v131, v131, s87, -0.5
	v_rcp_f32_e32 v141, v141
	v_add_f32_e32 v142, 1.0, v142
	v_cvt_pk_u8_f32 v131, v131, 0, 0
	v_fma_f32 v140, v140, s87, -0.5
	v_rcp_f32_e32 v142, v142
	v_add_f32_e32 v143, 1.0, v143
	v_cvt_pk_u8_f32 v131, v140, 1, v131
	v_fma_f32 v138, v138, s87, -0.5
	v_rcp_f32_e32 v143, v143
	v_cvt_pk_u8_f32 v131, v138, 2, v131
	v_fma_f32 v138, v139, s87, -0.5
	v_cvt_pk_u8_f32 v138, v138, 3, v131
	v_fma_f32 v131, v135, s87, -0.5
	v_cvt_pk_u8_f32 v131, v131, 0, 0
	v_fma_f32 v135, v141, s87, -0.5
	v_cvt_pk_u8_f32 v131, v135, 1, v131
	v_fma_f32 v135, v142, s87, -0.5
	v_cvt_pk_u8_f32 v131, v135, 2, v131
	v_fma_f32 v135, v143, s87, -0.5
	v_cvt_pk_u8_f32 v139, v135, 3, v131
	v_lshl_add_u64 v[136:137], v[136:137], 0, v[132:133]
	global_store_dwordx2 v[136:137], v[138:139], off
	v_mul_f32_e32 v135, 0xbd38aa3b, v18
	v_exp_f32_e32 v135, v135
	v_mul_f32_e32 v139, 0xbd38aa3b, v19
	v_exp_f32_e32 v139, v139
	v_mul_f32_e32 v136, 0xbd38aa3b, v20
	v_exp_f32_e32 v136, v136
	v_mul_f32_e32 v137, 0xbd38aa3b, v21
	v_mul_f32_e32 v138, 0xbd38aa3b, v10
	v_exp_f32_e32 v137, v137
	v_exp_f32_e32 v138, v138
	v_add_f32_e32 v135, 1.0, v135
	v_mul_f32_e32 v140, 0xbd38aa3b, v11
	v_rcp_f32_e32 v135, v135
	v_exp_f32_e32 v140, v140
	v_add_f32_e32 v139, 1.0, v139
	v_mul_f32_e32 v141, 0xbd38aa3b, v12
	v_rcp_f32_e32 v139, v139
	v_exp_f32_e32 v141, v141
	v_add_f32_e32 v136, 1.0, v136
	v_mul_f32_e32 v142, 0xbd38aa3b, v13
	v_rcp_f32_e32 v136, v136
	v_exp_f32_e32 v142, v142
	v_add_f32_e32 v137, 1.0, v137
	v_add_f32_e32 v138, 1.0, v138
	v_rcp_f32_e32 v137, v137
	v_rcp_f32_e32 v138, v138
	v_add_f32_e32 v140, 1.0, v140
	v_fma_f32 v135, v135, s87, -0.5
	v_rcp_f32_e32 v140, v140
	v_add_f32_e32 v141, 1.0, v141
	v_cvt_pk_u8_f32 v135, v135, 0, 0
	v_fma_f32 v139, v139, s87, -0.5
	v_rcp_f32_e32 v141, v141
	v_add_f32_e32 v142, 1.0, v142
	v_cvt_pk_u8_f32 v135, v139, 1, v135
	v_fma_f32 v136, v136, s87, -0.5
	v_add_u32_e32 v130, 0xb0, v130
	v_rcp_f32_e32 v142, v142
	v_cvt_pk_u8_f32 v135, v136, 2, v135
	v_fma_f32 v136, v137, s87, -0.5
	v_ashrrev_i32_e32 v131, 31, v130
	v_cvt_pk_u8_f32 v136, v136, 3, v135
	v_fma_f32 v135, v138, s87, -0.5
	v_lshlrev_b64 v[130:131], 11, v[130:131]
	v_cvt_pk_u8_f32 v135, v135, 0, 0
	v_fma_f32 v137, v140, s87, -0.5
	v_lshl_add_u64 v[130:131], s[22:23], 0, v[130:131]
	v_cvt_pk_u8_f32 v135, v137, 1, v135
	v_fma_f32 v137, v141, s87, -0.5
	v_lshl_add_u64 v[130:131], v[130:131], 0, s[24:25]
	v_cvt_pk_u8_f32 v135, v137, 2, v135
	v_fma_f32 v137, v142, s87, -0.5
	v_cvt_pk_u8_f32 v137, v137, 3, v135
	v_lshl_add_u64 v[138:139], v[130:131], 0, v[0:1]
	global_store_dwordx2 v[138:139], v[136:137], off
	v_mul_f32_e32 v0, 0xbd38aa3b, v6
	v_exp_f32_e32 v0, v0
	v_mul_f32_e32 v138, 0xbd38aa3b, v7
	v_exp_f32_e32 v138, v138
	v_mul_f32_e32 v136, 0xbd38aa3b, v8
	v_exp_f32_e32 v136, v136
	v_mul_f32_e32 v137, 0xbd38aa3b, v9
	v_mul_f32_e32 v135, 0xbd38aa3b, v2
	v_exp_f32_e32 v137, v137
	v_exp_f32_e32 v135, v135
	v_add_f32_e32 v0, 1.0, v0
	v_mul_f32_e32 v139, 0xbd38aa3b, v3
	v_rcp_f32_e32 v0, v0
	v_exp_f32_e32 v139, v139
	v_add_f32_e32 v138, 1.0, v138
	v_mul_f32_e32 v140, 0xbd38aa3b, v4
	v_rcp_f32_e32 v138, v138
	v_exp_f32_e32 v140, v140
	v_add_f32_e32 v136, 1.0, v136
	v_mul_f32_e32 v141, 0xbd38aa3b, v5
	v_rcp_f32_e32 v136, v136
	v_exp_f32_e32 v141, v141
	v_add_f32_e32 v137, 1.0, v137
	v_add_f32_e32 v135, 1.0, v135
	v_rcp_f32_e32 v137, v137
	v_rcp_f32_e32 v135, v135
	v_add_f32_e32 v139, 1.0, v139
	v_fma_f32 v0, v0, s87, -0.5
	v_rcp_f32_e32 v139, v139
	v_add_f32_e32 v140, 1.0, v140
	v_cvt_pk_u8_f32 v0, v0, 0, 0
	v_fma_f32 v138, v138, s87, -0.5
	v_rcp_f32_e32 v140, v140
	v_add_f32_e32 v141, 1.0, v141
	v_cvt_pk_u8_f32 v0, v138, 1, v0
	v_fma_f32 v136, v136, s87, -0.5
	v_rcp_f32_e32 v141, v141
	v_cvt_pk_u8_f32 v0, v136, 2, v0
	v_fma_f32 v136, v137, s87, -0.5
	v_cvt_pk_u8_f32 v136, v136, 3, v0
	v_fma_f32 v0, v135, s87, -0.5
	v_cvt_pk_u8_f32 v0, v0, 0, 0
	v_fma_f32 v135, v139, s87, -0.5
	v_cvt_pk_u8_f32 v0, v135, 1, v0
	v_fma_f32 v135, v140, s87, -0.5
	v_cvt_pk_u8_f32 v0, v135, 2, v0
	v_fma_f32 v135, v141, s87, -0.5
	v_cvt_pk_u8_f32 v137, v135, 3, v0
	v_lshl_add_u64 v[130:131], v[130:131], 0, v[132:133]
	global_store_dwordx2 v[130:131], v[136:137], off
	s_mov_b64 s[22:23], 0

.LBB0_598:
	s_mov_b32 s1, -1
	s_cmp_gt_i32 s0, 1
	v_mbcnt_lo_u32_b32 v0, s1, 0
	v_mbcnt_hi_u32_b32 v0, s1, v0
	v_and_b32_e32 v172, 15, v0
	v_bfe_u32 v134, v0, 4, 2
	s_mov_b64 s[22:23], -1
	v_mov_b32_e32 v240, v243
	s_cbranch_scc0 .LBB0_605
	s_cmp_gt_u32 s0, 3
	s_cbranch_scc0 .LBB0_601
	s_mov_b64 s[22:23], s[96:97]
	s_load_dwordx2 s[22:23], s[22:23], 0xe8
	s_lshl_b32 s1, s20, 8
	s_add_i32 s1, s1, s46
	v_or_b32_e32 v130, s1, v172
	v_ashrrev_i32_e32 v131, 31, v130
	v_lshlrev_b64 v[132:133], 11, v[130:131]
	s_waitcnt lgkmcnt(0)
	v_lshl_add_u64 v[132:133], s[22:23], 0, v[132:133]
	s_mov_b64 s[24:25], 0xbcaffc00
	v_mul_f32_e32 v131, 0xbd38aa3b, v126
	v_lshl_add_u64 v[136:137], v[132:133], 0, s[24:25]
	v_exp_f32_e32 v131, v131
	v_mul_f32_e32 v138, 0xbd38aa3b, v127
	v_exp_f32_e32 v138, v138
	v_mul_f32_e32 v132, 0xbd38aa3b, v128
	v_exp_f32_e32 v132, v132
	v_mul_f32_e32 v133, 0xbd38aa3b, v129
	v_mul_f32_e32 v135, 0xbd38aa3b, v122
	v_exp_f32_e32 v133, v133
	v_exp_f32_e32 v135, v135
	v_add_f32_e32 v131, 1.0, v131
	v_mul_f32_e32 v139, 0xbd38aa3b, v123
	v_rcp_f32_e32 v131, v131
	v_exp_f32_e32 v139, v139
	v_add_f32_e32 v138, 1.0, v138
	v_mul_f32_e32 v140, 0xbd38aa3b, v124
	v_rcp_f32_e32 v138, v138
	v_exp_f32_e32 v140, v140
	v_add_f32_e32 v132, 1.0, v132
	v_mul_f32_e32 v141, 0xbd38aa3b, v125
	v_rcp_f32_e32 v132, v132
	v_exp_f32_e32 v141, v141
	v_add_f32_e32 v133, 1.0, v133
	v_add_f32_e32 v135, 1.0, v135
	v_rcp_f32_e32 v133, v133
	v_rcp_f32_e32 v135, v135
	v_add_f32_e32 v139, 1.0, v139
	v_fma_f32 v131, v131, s87, -0.5
	v_rcp_f32_e32 v139, v139
	v_add_f32_e32 v140, 1.0, v140
	v_cvt_pk_u8_f32 v131, v131, 0, 0
	v_fma_f32 v138, v138, s87, -0.5
	v_rcp_f32_e32 v140, v140
	v_add_f32_e32 v141, 1.0, v141
	v_cvt_pk_u8_f32 v131, v138, 1, v131
	v_fma_f32 v132, v132, s87, -0.5
	v_rcp_f32_e32 v141, v141
	v_cvt_pk_u8_f32 v131, v132, 2, v131
	v_fma_f32 v132, v133, s87, -0.5
	v_cvt_pk_u8_f32 v132, v132, 3, v131
	v_fma_f32 v131, v135, s87, -0.5
	s_lshl_b32 s1, s0, 8
	v_cvt_pk_u8_f32 v131, v131, 0, 0
	v_fma_f32 v133, v139, s87, -0.5
	v_lshl_or_b32 v0, v134, 3, s1
	v_cvt_pk_u8_f32 v131, v133, 1, v131
	v_fma_f32 v133, v140, s87, -0.5
	v_or_b32_e32 v0, s47, v0
	v_cvt_pk_u8_f32 v131, v133, 2, v131
	v_fma_f32 v133, v141, s87, -0.5
	v_cvt_pk_u8_f32 v133, v133, 3, v131
	v_lshl_add_u64 v[138:139], v[136:137], 0, v[0:1]
	global_store_dwordx2 v[138:139], v[132:133], off
	v_mul_f32_e32 v131, 0xbd38aa3b, v118
	v_exp_f32_e32 v131, v131
	v_mul_f32_e32 v138, 0xbd38aa3b, v119
	v_exp_f32_e32 v138, v138
	v_mul_f32_e32 v132, 0xbd38aa3b, v120
	v_exp_f32_e32 v132, v132
	v_mul_f32_e32 v133, 0xbd38aa3b, v121
	v_mul_f32_e32 v135, 0xbd38aa3b, v114
	v_exp_f32_e32 v133, v133
	v_exp_f32_e32 v135, v135
	v_add_f32_e32 v131, 1.0, v131
	v_mul_f32_e32 v139, 0xbd38aa3b, v115
	v_rcp_f32_e32 v131, v131
	v_exp_f32_e32 v139, v139
	v_add_f32_e32 v138, 1.0, v138
	v_mul_f32_e32 v140, 0xbd38aa3b, v116
	v_rcp_f32_e32 v138, v138
	v_exp_f32_e32 v140, v140
	v_add_f32_e32 v132, 1.0, v132
	v_mul_f32_e32 v141, 0xbd38aa3b, v117
	v_rcp_f32_e32 v132, v132
	v_exp_f32_e32 v141, v141
	v_add_f32_e32 v133, 1.0, v133
	v_add_f32_e32 v135, 1.0, v135
	v_rcp_f32_e32 v133, v133
	v_rcp_f32_e32 v135, v135
	v_add_f32_e32 v139, 1.0, v139
	v_fma_f32 v131, v131, s87, -0.5
	v_rcp_f32_e32 v139, v139
	v_add_f32_e32 v140, 1.0, v140
	v_cvt_pk_u8_f32 v131, v131, 0, 0
	v_fma_f32 v138, v138, s87, -0.5
	v_rcp_f32_e32 v140, v140
	v_add_f32_e32 v141, 1.0, v141
	v_cvt_pk_u8_f32 v131, v138, 1, v131
	v_fma_f32 v132, v132, s87, -0.5
	v_rcp_f32_e32 v141, v141
	v_cvt_pk_u8_f32 v131, v132, 2, v131
	v_fma_f32 v132, v133, s87, -0.5
	v_cvt_pk_u8_f32 v138, v132, 3, v131
	v_fma_f32 v131, v135, s87, -0.5
	v_cvt_pk_u8_f32 v131, v131, 0, 0
	v_fma_f32 v132, v139, s87, -0.5
	v_cvt_pk_u8_f32 v131, v132, 1, v131
	v_fma_f32 v132, v140, s87, -0.5
	v_cvt_pk_u8_f32 v131, v132, 2, v131
	v_fma_f32 v132, v141, s87, -0.5
	v_cvt_pk_u8_f32 v139, v132, 3, v131
	v_or_b32_e32 v132, 0x80, v0
	v_mov_b32_e32 v133, v1
	v_lshl_add_u64 v[136:137], v[136:137], 0, v[132:133]
	v_mul_f32_e32 v131, 0xbd38aa3b, v110
	global_store_dwordx2 v[136:137], v[138:139], off
	v_exp_f32_e32 v131, v131
	v_mul_f32_e32 v140, 0xbd38aa3b, v111
	v_exp_f32_e32 v140, v140
	v_mul_f32_e32 v138, 0xbd38aa3b, v112
	v_exp_f32_e32 v138, v138
	v_mul_f32_e32 v139, 0xbd38aa3b, v113
	v_mul_f32_e32 v135, 0xbd38aa3b, v106
	v_exp_f32_e32 v139, v139
	v_exp_f32_e32 v135, v135
	v_add_f32_e32 v131, 1.0, v131
	v_mul_f32_e32 v141, 0xbd38aa3b, v107
	v_rcp_f32_e32 v131, v131
	v_exp_f32_e32 v141, v141
	v_add_f32_e32 v140, 1.0, v140
	v_mul_f32_e32 v142, 0xbd38aa3b, v108
	v_rcp_f32_e32 v140, v140
	v_exp_f32_e32 v142, v142
	v_add_f32_e32 v138, 1.0, v138
	v_mul_f32_e32 v143, 0xbd38aa3b, v109
	v_rcp_f32_e32 v138, v138
	v_exp_f32_e32 v143, v143
	v_add_f32_e32 v139, 1.0, v139
	v_add_f32_e32 v135, 1.0, v135
	v_rcp_f32_e32 v139, v139
	v_rcp_f32_e32 v135, v135
	v_add_f32_e32 v141, 1.0, v141
	v_fma_f32 v131, v131, s87, -0.5
	v_rcp_f32_e32 v141, v141
	v_add_f32_e32 v142, 1.0, v142
	v_cvt_pk_u8_f32 v131, v131, 0, 0
	v_fma_f32 v140, v140, s87, -0.5
	v_rcp_f32_e32 v142, v142
	v_add_f32_e32 v143, 1.0, v143
	v_cvt_pk_u8_f32 v131, v140, 1, v131
	v_fma_f32 v138, v138, s87, -0.5
	v_or_b32_e32 v136, 16, v130
	v_rcp_f32_e32 v143, v143
	v_cvt_pk_u8_f32 v131, v138, 2, v131
	v_fma_f32 v138, v139, s87, -0.5
	v_ashrrev_i32_e32 v137, 31, v136
	v_cvt_pk_u8_f32 v138, v138, 3, v131
	v_fma_f32 v131, v135, s87, -0.5
	v_lshlrev_b64 v[136:137], 11, v[136:137]
	v_cvt_pk_u8_f32 v131, v131, 0, 0
	v_fma_f32 v135, v141, s87, -0.5
	v_lshl_add_u64 v[136:137], s[22:23], 0, v[136:137]
	v_cvt_pk_u8_f32 v131, v135, 1, v131
	v_fma_f32 v135, v142, s87, -0.5
	v_lshl_add_u64 v[136:137], v[136:137], 0, s[24:25]
	v_cvt_pk_u8_f32 v131, v135, 2, v131
	v_fma_f32 v135, v143, s87, -0.5
	v_cvt_pk_u8_f32 v139, v135, 3, v131
	v_lshl_add_u64 v[140:141], v[136:137], 0, v[0:1]
	global_store_dwordx2 v[140:141], v[138:139], off
	v_mul_f32_e32 v131, 0xbd38aa3b, v102
	v_exp_f32_e32 v131, v131
	v_mul_f32_e32 v140, 0xbd38aa3b, v103
	v_exp_f32_e32 v140, v140
	v_mul_f32_e32 v138, 0xbd38aa3b, v104
	v_exp_f32_e32 v138, v138
	v_mul_f32_e32 v139, 0xbd38aa3b, v105
	v_mul_f32_e32 v135, 0xbd38aa3b, v94
	v_exp_f32_e32 v139, v139
	v_exp_f32_e32 v135, v135
	v_add_f32_e32 v131, 1.0, v131
	v_mul_f32_e32 v141, 0xbd38aa3b, v95
	v_rcp_f32_e32 v131, v131
	v_exp_f32_e32 v141, v141
	v_add_f32_e32 v140, 1.0, v140
	v_mul_f32_e32 v142, 0xbd38aa3b, v96
	v_rcp_f32_e32 v140, v140
	v_exp_f32_e32 v142, v142
	v_add_f32_e32 v138, 1.0, v138
	v_mul_f32_e32 v143, 0xbd38aa3b, v97
	v_rcp_f32_e32 v138, v138
	v_exp_f32_e32 v143, v143
	v_add_f32_e32 v139, 1.0, v139
	v_add_f32_e32 v135, 1.0, v135
	v_rcp_f32_e32 v139, v139
	v_rcp_f32_e32 v135, v135
	v_add_f32_e32 v141, 1.0, v141
	v_fma_f32 v131, v131, s87, -0.5
	v_rcp_f32_e32 v141, v141
	v_add_f32_e32 v142, 1.0, v142
	v_cvt_pk_u8_f32 v131, v131, 0, 0
	v_fma_f32 v140, v140, s87, -0.5
	v_rcp_f32_e32 v142, v142
	v_add_f32_e32 v143, 1.0, v143
	v_cvt_pk_u8_f32 v131, v140, 1, v131
	v_fma_f32 v138, v138, s87, -0.5
	v_rcp_f32_e32 v143, v143
	v_cvt_pk_u8_f32 v131, v138, 2, v131
	v_fma_f32 v138, v139, s87, -0.5
	v_cvt_pk_u8_f32 v138, v138, 3, v131
	v_fma_f32 v131, v135, s87, -0.5
	v_cvt_pk_u8_f32 v131, v131, 0, 0
	v_fma_f32 v135, v141, s87, -0.5
	v_cvt_pk_u8_f32 v131, v135, 1, v131
	v_fma_f32 v135, v142, s87, -0.5
	v_cvt_pk_u8_f32 v131, v135, 2, v131
	v_fma_f32 v135, v143, s87, -0.5
	v_cvt_pk_u8_f32 v139, v135, 3, v131
	v_lshl_add_u64 v[136:137], v[136:137], 0, v[132:133]
	v_mul_f32_e32 v131, 0xbd38aa3b, v98
	global_store_dwordx2 v[136:137], v[138:139], off
	v_exp_f32_e32 v131, v131
	v_mul_f32_e32 v140, 0xbd38aa3b, v99
	v_exp_f32_e32 v140, v140
	v_mul_f32_e32 v138, 0xbd38aa3b, v100
	v_exp_f32_e32 v138, v138
	v_mul_f32_e32 v139, 0xbd38aa3b, v101
	v_mul_f32_e32 v135, 0xbd38aa3b, v90
	v_exp_f32_e32 v139, v139
	v_exp_f32_e32 v135, v135
	v_add_f32_e32 v131, 1.0, v131
	v_mul_f32_e32 v141, 0xbd38aa3b, v91
	v_rcp_f32_e32 v131, v131
	v_exp_f32_e32 v141, v141
	v_add_f32_e32 v140, 1.0, v140
	v_mul_f32_e32 v142, 0xbd38aa3b, v92
	v_rcp_f32_e32 v140, v140
	v_exp_f32_e32 v142, v142
	v_add_f32_e32 v138, 1.0, v138
	v_mul_f32_e32 v143, 0xbd38aa3b, v93
	v_rcp_f32_e32 v138, v138
	v_exp_f32_e32 v143, v143
	v_add_f32_e32 v139, 1.0, v139
	v_add_f32_e32 v135, 1.0, v135
	v_rcp_f32_e32 v139, v139
	v_rcp_f32_e32 v135, v135
	v_add_f32_e32 v141, 1.0, v141
	v_fma_f32 v131, v131, s87, -0.5
	v_rcp_f32_e32 v141, v141
	v_add_f32_e32 v142, 1.0, v142
	v_cvt_pk_u8_f32 v131, v131, 0, 0
	v_fma_f32 v140, v140, s87, -0.5
	v_rcp_f32_e32 v142, v142
	v_add_f32_e32 v143, 1.0, v143
	v_cvt_pk_u8_f32 v131, v140, 1, v131
	v_fma_f32 v138, v138, s87, -0.5
	v_or_b32_e32 v136, 32, v130
	v_rcp_f32_e32 v143, v143
	v_cvt_pk_u8_f32 v131, v138, 2, v131
	v_fma_f32 v138, v139, s87, -0.5
	v_ashrrev_i32_e32 v137, 31, v136
	v_cvt_pk_u8_f32 v138, v138, 3, v131
	v_fma_f32 v131, v135, s87, -0.5
	v_lshlrev_b64 v[136:137], 11, v[136:137]
	v_cvt_pk_u8_f32 v131, v131, 0, 0
	v_fma_f32 v135, v141, s87, -0.5
	v_lshl_add_u64 v[136:137], s[22:23], 0, v[136:137]
	v_cvt_pk_u8_f32 v131, v135, 1, v131
	v_fma_f32 v135, v142, s87, -0.5
	v_lshl_add_u64 v[136:137], v[136:137], 0, s[24:25]
	v_cvt_pk_u8_f32 v131, v135, 2, v131
	v_fma_f32 v135, v143, s87, -0.5
	v_cvt_pk_u8_f32 v139, v135, 3, v131
	v_lshl_add_u64 v[140:141], v[136:137], 0, v[0:1]
	global_store_dwordx2 v[140:141], v[138:139], off
	v_mul_f32_e32 v131, 0xbd38aa3b, v86
	v_exp_f32_e32 v131, v131
	v_mul_f32_e32 v140, 0xbd38aa3b, v87
	v_exp_f32_e32 v140, v140
	v_mul_f32_e32 v138, 0xbd38aa3b, v88
	v_exp_f32_e32 v138, v138
	v_mul_f32_e32 v139, 0xbd38aa3b, v89
	v_mul_f32_e32 v135, 0xbd38aa3b, v78
	v_exp_f32_e32 v139, v139
	v_exp_f32_e32 v135, v135
	v_add_f32_e32 v131, 1.0, v131
	v_mul_f32_e32 v141, 0xbd38aa3b, v79
	v_rcp_f32_e32 v131, v131
	v_exp_f32_e32 v141, v141
	v_add_f32_e32 v140, 1.0, v140
	v_mul_f32_e32 v142, 0xbd38aa3b, v80
	v_rcp_f32_e32 v140, v140
	v_exp_f32_e32 v142, v142
	v_add_f32_e32 v138, 1.0, v138
	v_mul_f32_e32 v143, 0xbd38aa3b, v81
	v_rcp_f32_e32 v138, v138
	v_exp_f32_e32 v143, v143
	v_add_f32_e32 v139, 1.0, v139
	v_add_f32_e32 v135, 1.0, v135
	v_rcp_f32_e32 v139, v139
	v_rcp_f32_e32 v135, v135
	v_add_f32_e32 v141, 1.0, v141
	v_fma_f32 v131, v131, s87, -0.5
	v_rcp_f32_e32 v141, v141
	v_add_f32_e32 v142, 1.0, v142
	v_cvt_pk_u8_f32 v131, v131, 0, 0
	v_fma_f32 v140, v140, s87, -0.5
	v_rcp_f32_e32 v142, v142
	v_add_f32_e32 v143, 1.0, v143
	v_cvt_pk_u8_f32 v131, v140, 1, v131
	v_fma_f32 v138, v138, s87, -0.5
	v_rcp_f32_e32 v143, v143
	v_cvt_pk_u8_f32 v131, v138, 2, v131
	v_fma_f32 v138, v139, s87, -0.5
	v_cvt_pk_u8_f32 v138, v138, 3, v131
	v_fma_f32 v131, v135, s87, -0.5
	v_cvt_pk_u8_f32 v131, v131, 0, 0
	v_fma_f32 v135, v141, s87, -0.5
	v_cvt_pk_u8_f32 v131, v135, 1, v131
	v_fma_f32 v135, v142, s87, -0.5
	v_cvt_pk_u8_f32 v131, v135, 2, v131
	v_fma_f32 v135, v143, s87, -0.5
	v_cvt_pk_u8_f32 v139, v135, 3, v131
	v_lshl_add_u64 v[136:137], v[136:137], 0, v[132:133]
	v_mul_f32_e32 v131, 0xbd38aa3b, v82
	global_store_dwordx2 v[136:137], v[138:139], off
	v_exp_f32_e32 v131, v131
	v_mul_f32_e32 v140, 0xbd38aa3b, v83
	v_exp_f32_e32 v140, v140
	v_mul_f32_e32 v138, 0xbd38aa3b, v84
	v_exp_f32_e32 v138, v138
	v_mul_f32_e32 v139, 0xbd38aa3b, v85
	v_mul_f32_e32 v135, 0xbd38aa3b, v74
	v_exp_f32_e32 v139, v139
	v_exp_f32_e32 v135, v135
	v_add_f32_e32 v131, 1.0, v131
	v_mul_f32_e32 v141, 0xbd38aa3b, v75
	v_rcp_f32_e32 v131, v131
	v_exp_f32_e32 v141, v141
	v_add_f32_e32 v140, 1.0, v140
	v_mul_f32_e32 v142, 0xbd38aa3b, v76
	v_rcp_f32_e32 v140, v140
	v_exp_f32_e32 v142, v142
	v_add_f32_e32 v138, 1.0, v138
	v_mul_f32_e32 v143, 0xbd38aa3b, v77
	v_rcp_f32_e32 v138, v138
	v_exp_f32_e32 v143, v143
	v_add_f32_e32 v139, 1.0, v139
	v_add_f32_e32 v135, 1.0, v135
	v_rcp_f32_e32 v139, v139
	v_rcp_f32_e32 v135, v135
	v_add_f32_e32 v141, 1.0, v141
	v_fma_f32 v131, v131, s87, -0.5
	v_rcp_f32_e32 v141, v141
	v_add_f32_e32 v142, 1.0, v142
	v_cvt_pk_u8_f32 v131, v131, 0, 0
	v_fma_f32 v140, v140, s87, -0.5
	v_rcp_f32_e32 v142, v142
	v_add_f32_e32 v143, 1.0, v143
	v_cvt_pk_u8_f32 v131, v140, 1, v131
	v_fma_f32 v138, v138, s87, -0.5
	v_or_b32_e32 v136, 48, v130
	v_rcp_f32_e32 v143, v143
	v_cvt_pk_u8_f32 v131, v138, 2, v131
	v_fma_f32 v138, v139, s87, -0.5
	v_ashrrev_i32_e32 v137, 31, v136
	v_cvt_pk_u8_f32 v138, v138, 3, v131
	v_fma_f32 v131, v135, s87, -0.5
	v_lshlrev_b64 v[136:137], 11, v[136:137]
	v_cvt_pk_u8_f32 v131, v131, 0, 0
	v_fma_f32 v135, v141, s87, -0.5
	v_lshl_add_u64 v[136:137], s[22:23], 0, v[136:137]
	v_cvt_pk_u8_f32 v131, v135, 1, v131
	v_fma_f32 v135, v142, s87, -0.5
	v_lshl_add_u64 v[136:137], v[136:137], 0, s[24:25]
	v_cvt_pk_u8_f32 v131, v135, 2, v131
	v_fma_f32 v135, v143, s87, -0.5
	v_cvt_pk_u8_f32 v139, v135, 3, v131
	v_lshl_add_u64 v[140:141], v[136:137], 0, v[0:1]
	global_store_dwordx2 v[140:141], v[138:139], off
	v_mul_f32_e32 v131, 0xbd38aa3b, v70
	v_exp_f32_e32 v131, v131
	v_mul_f32_e32 v140, 0xbd38aa3b, v71
	v_exp_f32_e32 v140, v140
	v_mul_f32_e32 v138, 0xbd38aa3b, v72
	v_exp_f32_e32 v138, v138
	v_mul_f32_e32 v139, 0xbd38aa3b, v73
	v_mul_f32_e32 v135, 0xbd38aa3b, v66
	v_exp_f32_e32 v139, v139
	v_exp_f32_e32 v135, v135
	v_add_f32_e32 v131, 1.0, v131
	v_mul_f32_e32 v141, 0xbd38aa3b, v67
	v_rcp_f32_e32 v131, v131
	v_exp_f32_e32 v141, v141
	v_add_f32_e32 v140, 1.0, v140
	v_mul_f32_e32 v142, 0xbd38aa3b, v68
	v_rcp_f32_e32 v140, v140
	v_exp_f32_e32 v142, v142
	v_add_f32_e32 v138, 1.0, v138
	v_mul_f32_e32 v143, 0xbd38aa3b, v69
	v_rcp_f32_e32 v138, v138
	v_exp_f32_e32 v143, v143
	v_add_f32_e32 v139, 1.0, v139
	v_add_f32_e32 v135, 1.0, v135
	v_rcp_f32_e32 v139, v139
	v_rcp_f32_e32 v135, v135
	v_add_f32_e32 v141, 1.0, v141
	v_fma_f32 v131, v131, s87, -0.5
	v_rcp_f32_e32 v141, v141
	v_add_f32_e32 v142, 1.0, v142
	v_cvt_pk_u8_f32 v131, v131, 0, 0
	v_fma_f32 v140, v140, s87, -0.5
	v_rcp_f32_e32 v142, v142
	v_add_f32_e32 v143, 1.0, v143
	v_cvt_pk_u8_f32 v131, v140, 1, v131
	v_fma_f32 v138, v138, s87, -0.5
	v_rcp_f32_e32 v143, v143
	v_cvt_pk_u8_f32 v131, v138, 2, v131
	v_fma_f32 v138, v139, s87, -0.5
	v_cvt_pk_u8_f32 v138, v138, 3, v131
	v_fma_f32 v131, v135, s87, -0.5
	v_cvt_pk_u8_f32 v131, v131, 0, 0
	v_fma_f32 v135, v141, s87, -0.5
	v_cvt_pk_u8_f32 v131, v135, 1, v131
	v_fma_f32 v135, v142, s87, -0.5
	v_cvt_pk_u8_f32 v131, v135, 2, v131
	v_fma_f32 v135, v143, s87, -0.5
	v_cvt_pk_u8_f32 v139, v135, 3, v131
	v_lshl_add_u64 v[136:137], v[136:137], 0, v[132:133]
	v_mul_f32_e32 v131, 0xbd38aa3b, v62
	global_store_dwordx2 v[136:137], v[138:139], off
	v_exp_f32_e32 v131, v131
	v_mul_f32_e32 v140, 0xbd38aa3b, v63
	v_exp_f32_e32 v140, v140
	v_mul_f32_e32 v138, 0xbd38aa3b, v64
	v_exp_f32_e32 v138, v138
	v_mul_f32_e32 v139, 0xbd38aa3b, v65
	v_mul_f32_e32 v135, 0xbd38aa3b, v58
	v_exp_f32_e32 v139, v139
	v_exp_f32_e32 v135, v135
	v_add_f32_e32 v131, 1.0, v131
	v_mul_f32_e32 v141, 0xbd38aa3b, v59
	v_rcp_f32_e32 v131, v131
	v_exp_f32_e32 v141, v141
	v_add_f32_e32 v140, 1.0, v140
	v_mul_f32_e32 v142, 0xbd38aa3b, v60
	v_rcp_f32_e32 v140, v140
	v_exp_f32_e32 v142, v142
	v_add_f32_e32 v138, 1.0, v138
	v_mul_f32_e32 v143, 0xbd38aa3b, v61
	v_rcp_f32_e32 v138, v138
	v_exp_f32_e32 v143, v143
	v_add_f32_e32 v139, 1.0, v139
	v_add_f32_e32 v135, 1.0, v135
	v_rcp_f32_e32 v139, v139
	v_rcp_f32_e32 v135, v135
	v_add_f32_e32 v141, 1.0, v141
	v_fma_f32 v131, v131, s87, -0.5
	v_rcp_f32_e32 v141, v141
	v_add_f32_e32 v142, 1.0, v142
	v_cvt_pk_u8_f32 v131, v131, 0, 0
	v_fma_f32 v140, v140, s87, -0.5
	v_rcp_f32_e32 v142, v142
	v_add_f32_e32 v143, 1.0, v143
	v_cvt_pk_u8_f32 v131, v140, 1, v131
	v_fma_f32 v138, v138, s87, -0.5
	v_add_u32_e32 v136, 0x80, v130
	v_rcp_f32_e32 v143, v143
	v_cvt_pk_u8_f32 v131, v138, 2, v131
	v_fma_f32 v138, v139, s87, -0.5
	v_ashrrev_i32_e32 v137, 31, v136
	v_cvt_pk_u8_f32 v138, v138, 3, v131
	v_fma_f32 v131, v135, s87, -0.5
	v_lshlrev_b64 v[136:137], 11, v[136:137]
	v_cvt_pk_u8_f32 v131, v131, 0, 0
	v_fma_f32 v135, v141, s87, -0.5
	v_lshl_add_u64 v[136:137], s[22:23], 0, v[136:137]
	v_cvt_pk_u8_f32 v131, v135, 1, v131
	v_fma_f32 v135, v142, s87, -0.5
	v_lshl_add_u64 v[136:137], v[136:137], 0, s[24:25]
	v_cvt_pk_u8_f32 v131, v135, 2, v131
	v_fma_f32 v135, v143, s87, -0.5
	v_cvt_pk_u8_f32 v139, v135, 3, v131
	v_lshl_add_u64 v[140:141], v[136:137], 0, v[0:1]
	global_store_dwordx2 v[140:141], v[138:139], off
	v_mul_f32_e32 v131, 0xbd38aa3b, v54
	v_exp_f32_e32 v131, v131
	v_mul_f32_e32 v140, 0xbd38aa3b, v55
	v_exp_f32_e32 v140, v140
	v_mul_f32_e32 v138, 0xbd38aa3b, v56
	v_exp_f32_e32 v138, v138
	v_mul_f32_e32 v139, 0xbd38aa3b, v57
	v_mul_f32_e32 v135, 0xbd38aa3b, v46
	v_exp_f32_e32 v139, v139
	v_exp_f32_e32 v135, v135
	v_add_f32_e32 v131, 1.0, v131
	v_mul_f32_e32 v141, 0xbd38aa3b, v47
	v_rcp_f32_e32 v131, v131
	v_exp_f32_e32 v141, v141
	v_add_f32_e32 v140, 1.0, v140
	v_mul_f32_e32 v142, 0xbd38aa3b, v48
	v_rcp_f32_e32 v140, v140
	v_exp_f32_e32 v142, v142
	v_add_f32_e32 v138, 1.0, v138
	v_mul_f32_e32 v143, 0xbd38aa3b, v49
	v_rcp_f32_e32 v138, v138
	v_exp_f32_e32 v143, v143
	v_add_f32_e32 v139, 1.0, v139
	v_add_f32_e32 v135, 1.0, v135
	v_rcp_f32_e32 v139, v139
	v_rcp_f32_e32 v135, v135
	v_add_f32_e32 v141, 1.0, v141
	v_fma_f32 v131, v131, s87, -0.5
	v_rcp_f32_e32 v141, v141
	v_add_f32_e32 v142, 1.0, v142
	v_cvt_pk_u8_f32 v131, v131, 0, 0
	v_fma_f32 v140, v140, s87, -0.5
	v_rcp_f32_e32 v142, v142
	v_add_f32_e32 v143, 1.0, v143
	v_cvt_pk_u8_f32 v131, v140, 1, v131
	v_fma_f32 v138, v138, s87, -0.5
	v_rcp_f32_e32 v143, v143
	v_cvt_pk_u8_f32 v131, v138, 2, v131
	v_fma_f32 v138, v139, s87, -0.5
	v_cvt_pk_u8_f32 v138, v138, 3, v131
	v_fma_f32 v131, v135, s87, -0.5
	v_cvt_pk_u8_f32 v131, v131, 0, 0
	v_fma_f32 v135, v141, s87, -0.5
	v_cvt_pk_u8_f32 v131, v135, 1, v131
	v_fma_f32 v135, v142, s87, -0.5
	v_cvt_pk_u8_f32 v131, v135, 2, v131
	v_fma_f32 v135, v143, s87, -0.5
	v_cvt_pk_u8_f32 v139, v135, 3, v131
	v_lshl_add_u64 v[136:137], v[136:137], 0, v[132:133]
	v_mul_f32_e32 v131, 0xbd38aa3b, v50
	global_store_dwordx2 v[136:137], v[138:139], off
	v_exp_f32_e32 v131, v131
	v_mul_f32_e32 v140, 0xbd38aa3b, v51
	v_exp_f32_e32 v140, v140
	v_mul_f32_e32 v138, 0xbd38aa3b, v52
	v_exp_f32_e32 v138, v138
	v_mul_f32_e32 v139, 0xbd38aa3b, v53
	v_mul_f32_e32 v135, 0xbd38aa3b, v42
	v_exp_f32_e32 v139, v139
	v_exp_f32_e32 v135, v135
	v_add_f32_e32 v131, 1.0, v131
	v_mul_f32_e32 v141, 0xbd38aa3b, v43
	v_rcp_f32_e32 v131, v131
	v_exp_f32_e32 v141, v141
	v_add_f32_e32 v140, 1.0, v140
	v_mul_f32_e32 v142, 0xbd38aa3b, v44
	v_rcp_f32_e32 v140, v140
	v_exp_f32_e32 v142, v142
	v_add_f32_e32 v138, 1.0, v138
	v_mul_f32_e32 v143, 0xbd38aa3b, v45
	v_rcp_f32_e32 v138, v138
	v_exp_f32_e32 v143, v143
	v_add_f32_e32 v139, 1.0, v139
	v_add_f32_e32 v135, 1.0, v135
	v_rcp_f32_e32 v139, v139
	v_rcp_f32_e32 v135, v135
	v_add_f32_e32 v141, 1.0, v141
	v_fma_f32 v131, v131, s87, -0.5
	v_rcp_f32_e32 v141, v141
	v_add_f32_e32 v142, 1.0, v142
	v_cvt_pk_u8_f32 v131, v131, 0, 0
	v_fma_f32 v140, v140, s87, -0.5
	v_rcp_f32_e32 v142, v142
	v_add_f32_e32 v143, 1.0, v143
	v_cvt_pk_u8_f32 v131, v140, 1, v131
	v_fma_f32 v138, v138, s87, -0.5
	v_add_u32_e32 v136, 0x90, v130
	v_rcp_f32_e32 v143, v143
	v_cvt_pk_u8_f32 v131, v138, 2, v131
	v_fma_f32 v138, v139, s87, -0.5
	v_ashrrev_i32_e32 v137, 31, v136
	v_cvt_pk_u8_f32 v138, v138, 3, v131
	v_fma_f32 v131, v135, s87, -0.5
	v_lshlrev_b64 v[136:137], 11, v[136:137]
	v_cvt_pk_u8_f32 v131, v131, 0, 0
	v_fma_f32 v135, v141, s87, -0.5
	v_lshl_add_u64 v[136:137], s[22:23], 0, v[136:137]
	v_cvt_pk_u8_f32 v131, v135, 1, v131
	v_fma_f32 v135, v142, s87, -0.5
	v_lshl_add_u64 v[136:137], v[136:137], 0, s[24:25]
	v_cvt_pk_u8_f32 v131, v135, 2, v131
	v_fma_f32 v135, v143, s87, -0.5
	v_cvt_pk_u8_f32 v139, v135, 3, v131
	v_lshl_add_u64 v[140:141], v[136:137], 0, v[0:1]
	global_store_dwordx2 v[140:141], v[138:139], off
	v_mul_f32_e32 v131, 0xbd38aa3b, v38
	v_exp_f32_e32 v131, v131
	v_mul_f32_e32 v140, 0xbd38aa3b, v39
	v_exp_f32_e32 v140, v140
	v_mul_f32_e32 v138, 0xbd38aa3b, v40
	v_exp_f32_e32 v138, v138
	v_mul_f32_e32 v139, 0xbd38aa3b, v41
	v_mul_f32_e32 v135, 0xbd38aa3b, v30
	v_exp_f32_e32 v139, v139
	v_exp_f32_e32 v135, v135
	v_add_f32_e32 v131, 1.0, v131
	v_mul_f32_e32 v141, 0xbd38aa3b, v31
	v_rcp_f32_e32 v131, v131
	v_exp_f32_e32 v141, v141
	v_add_f32_e32 v140, 1.0, v140
	v_mul_f32_e32 v142, 0xbd38aa3b, v32
	v_rcp_f32_e32 v140, v140
	v_exp_f32_e32 v142, v142
	v_add_f32_e32 v138, 1.0, v138
	v_mul_f32_e32 v143, 0xbd38aa3b, v33
	v_rcp_f32_e32 v138, v138
	v_exp_f32_e32 v143, v143
	v_add_f32_e32 v139, 1.0, v139
	v_add_f32_e32 v135, 1.0, v135
	v_rcp_f32_e32 v139, v139
	v_rcp_f32_e32 v135, v135
	v_add_f32_e32 v141, 1.0, v141
	v_fma_f32 v131, v131, s87, -0.5
	v_rcp_f32_e32 v141, v141
	v_add_f32_e32 v142, 1.0, v142
	v_cvt_pk_u8_f32 v131, v131, 0, 0
	v_fma_f32 v140, v140, s87, -0.5
	v_rcp_f32_e32 v142, v142
	v_add_f32_e32 v143, 1.0, v143
	v_cvt_pk_u8_f32 v131, v140, 1, v131
	v_fma_f32 v138, v138, s87, -0.5
	v_rcp_f32_e32 v143, v143
	v_cvt_pk_u8_f32 v131, v138, 2, v131
	v_fma_f32 v138, v139, s87, -0.5
	v_cvt_pk_u8_f32 v138, v138, 3, v131
	v_fma_f32 v131, v135, s87, -0.5
	v_cvt_pk_u8_f32 v131, v131, 0, 0
	v_fma_f32 v135, v141, s87, -0.5
	v_cvt_pk_u8_f32 v131, v135, 1, v131
	v_fma_f32 v135, v142, s87, -0.5
	v_cvt_pk_u8_f32 v131, v135, 2, v131
	v_fma_f32 v135, v143, s87, -0.5
	v_cvt_pk_u8_f32 v139, v135, 3, v131
	v_lshl_add_u64 v[136:137], v[136:137], 0, v[132:133]
	v_mul_f32_e32 v131, 0xbd38aa3b, v34
	global_store_dwordx2 v[136:137], v[138:139], off
	v_exp_f32_e32 v131, v131
	v_mul_f32_e32 v140, 0xbd38aa3b, v35
	v_exp_f32_e32 v140, v140
	v_mul_f32_e32 v138, 0xbd38aa3b, v36
	v_exp_f32_e32 v138, v138
	v_mul_f32_e32 v139, 0xbd38aa3b, v37
	v_mul_f32_e32 v135, 0xbd38aa3b, v26
	v_exp_f32_e32 v139, v139
	v_exp_f32_e32 v135, v135
	v_add_f32_e32 v131, 1.0, v131
	v_mul_f32_e32 v141, 0xbd38aa3b, v27
	v_rcp_f32_e32 v131, v131
	v_exp_f32_e32 v141, v141
	v_add_f32_e32 v140, 1.0, v140
	v_mul_f32_e32 v142, 0xbd38aa3b, v28
	v_rcp_f32_e32 v140, v140
	v_exp_f32_e32 v142, v142
	v_add_f32_e32 v138, 1.0, v138
	v_mul_f32_e32 v143, 0xbd38aa3b, v29
	v_rcp_f32_e32 v138, v138
	v_exp_f32_e32 v143, v143
	v_add_f32_e32 v139, 1.0, v139
	v_add_f32_e32 v135, 1.0, v135
	v_rcp_f32_e32 v139, v139
	v_rcp_f32_e32 v135, v135
	v_add_f32_e32 v141, 1.0, v141
	v_fma_f32 v131, v131, s87, -0.5
	v_rcp_f32_e32 v141, v141
	v_add_f32_e32 v142, 1.0, v142
	v_cvt_pk_u8_f32 v131, v131, 0, 0
	v_fma_f32 v140, v140, s87, -0.5
	v_rcp_f32_e32 v142, v142
	v_add_f32_e32 v143, 1.0, v143
	v_cvt_pk_u8_f32 v131, v140, 1, v131
	v_fma_f32 v138, v138, s87, -0.5
	v_add_u32_e32 v136, 0xa0, v130
	v_rcp_f32_e32 v143, v143
	v_cvt_pk_u8_f32 v131, v138, 2, v131
	v_fma_f32 v138, v139, s87, -0.5
	v_ashrrev_i32_e32 v137, 31, v136
	v_cvt_pk_u8_f32 v138, v138, 3, v131
	v_fma_f32 v131, v135, s87, -0.5
	v_lshlrev_b64 v[136:137], 11, v[136:137]
	v_cvt_pk_u8_f32 v131, v131, 0, 0
	v_fma_f32 v135, v141, s87, -0.5
	v_lshl_add_u64 v[136:137], s[22:23], 0, v[136:137]
	v_cvt_pk_u8_f32 v131, v135, 1, v131
	v_fma_f32 v135, v142, s87, -0.5
	v_lshl_add_u64 v[136:137], v[136:137], 0, s[24:25]
	v_cvt_pk_u8_f32 v131, v135, 2, v131
	v_fma_f32 v135, v143, s87, -0.5
	v_cvt_pk_u8_f32 v139, v135, 3, v131
	v_lshl_add_u64 v[140:141], v[136:137], 0, v[0:1]
	global_store_dwordx2 v[140:141], v[138:139], off
	v_mul_f32_e32 v131, 0xbd38aa3b, v22
	v_exp_f32_e32 v131, v131
	v_mul_f32_e32 v140, 0xbd38aa3b, v23
	v_exp_f32_e32 v140, v140
	v_mul_f32_e32 v138, 0xbd38aa3b, v24
	v_exp_f32_e32 v138, v138
	v_mul_f32_e32 v139, 0xbd38aa3b, v25
	v_mul_f32_e32 v135, 0xbd38aa3b, v14
	v_exp_f32_e32 v139, v139
	v_exp_f32_e32 v135, v135
	v_add_f32_e32 v131, 1.0, v131
	v_mul_f32_e32 v141, 0xbd38aa3b, v15
	v_rcp_f32_e32 v131, v131
	v_exp_f32_e32 v141, v141
	v_add_f32_e32 v140, 1.0, v140
	v_mul_f32_e32 v142, 0xbd38aa3b, v16
	v_rcp_f32_e32 v140, v140
	v_exp_f32_e32 v142, v142
	v_add_f32_e32 v138, 1.0, v138
	v_mul_f32_e32 v143, 0xbd38aa3b, v17
	v_rcp_f32_e32 v138, v138
	v_exp_f32_e32 v143, v143
	v_add_f32_e32 v139, 1.0, v139
	v_add_f32_e32 v135, 1.0, v135
	v_rcp_f32_e32 v139, v139
	v_rcp_f32_e32 v135, v135
	v_add_f32_e32 v141, 1.0, v141
	v_fma_f32 v131, v131, s87, -0.5
	v_rcp_f32_e32 v141, v141
	v_add_f32_e32 v142, 1.0, v142
	v_cvt_pk_u8_f32 v131, v131, 0, 0
	v_fma_f32 v140, v140, s87, -0.5
	v_rcp_f32_e32 v142, v142
	v_add_f32_e32 v143, 1.0, v143
	v_cvt_pk_u8_f32 v131, v140, 1, v131
	v_fma_f32 v138, v138, s87, -0.5
	v_rcp_f32_e32 v143, v143
	v_cvt_pk_u8_f32 v131, v138, 2, v131
	v_fma_f32 v138, v139, s87, -0.5
	v_cvt_pk_u8_f32 v138, v138, 3, v131
	v_fma_f32 v131, v135, s87, -0.5
	v_cvt_pk_u8_f32 v131, v131, 0, 0
	v_fma_f32 v135, v141, s87, -0.5
	v_cvt_pk_u8_f32 v131, v135, 1, v131
	v_fma_f32 v135, v142, s87, -0.5
	v_cvt_pk_u8_f32 v131, v135, 2, v131
	v_fma_f32 v135, v143, s87, -0.5
	v_cvt_pk_u8_f32 v139, v135, 3, v131
	v_lshl_add_u64 v[136:137], v[136:137], 0, v[132:133]
	global_store_dwordx2 v[136:137], v[138:139], off
	v_mul_f32_e32 v135, 0xbd38aa3b, v18
	v_exp_f32_e32 v135, v135
	v_mul_f32_e32 v139, 0xbd38aa3b, v19
	v_exp_f32_e32 v139, v139
	v_mul_f32_e32 v136, 0xbd38aa3b, v20
	v_exp_f32_e32 v136, v136
	v_mul_f32_e32 v137, 0xbd38aa3b, v21
	v_mul_f32_e32 v138, 0xbd38aa3b, v10
	v_exp_f32_e32 v137, v137
	v_exp_f32_e32 v138, v138
	v_add_f32_e32 v135, 1.0, v135
	v_mul_f32_e32 v140, 0xbd38aa3b, v11
	v_rcp_f32_e32 v135, v135
	v_exp_f32_e32 v140, v140
	v_add_f32_e32 v139, 1.0, v139
	v_mul_f32_e32 v141, 0xbd38aa3b, v12
	v_rcp_f32_e32 v139, v139
	v_exp_f32_e32 v141, v141
	v_add_f32_e32 v136, 1.0, v136
	v_mul_f32_e32 v142, 0xbd38aa3b, v13
	v_rcp_f32_e32 v136, v136
	v_exp_f32_e32 v142, v142
	v_add_f32_e32 v137, 1.0, v137
	v_add_f32_e32 v138, 1.0, v138
	v_rcp_f32_e32 v137, v137
	v_rcp_f32_e32 v138, v138
	v_add_f32_e32 v140, 1.0, v140
	v_fma_f32 v135, v135, s87, -0.5
	v_rcp_f32_e32 v140, v140
	v_add_f32_e32 v141, 1.0, v141
	v_cvt_pk_u8_f32 v135, v135, 0, 0
	v_fma_f32 v139, v139, s87, -0.5
	v_rcp_f32_e32 v141, v141
	v_add_f32_e32 v142, 1.0, v142
	v_cvt_pk_u8_f32 v135, v139, 1, v135
	v_fma_f32 v136, v136, s87, -0.5
	v_add_u32_e32 v130, 0xb0, v130
	v_rcp_f32_e32 v142, v142
	v_cvt_pk_u8_f32 v135, v136, 2, v135
	v_fma_f32 v136, v137, s87, -0.5
	v_ashrrev_i32_e32 v131, 31, v130
	v_cvt_pk_u8_f32 v136, v136, 3, v135
	v_fma_f32 v135, v138, s87, -0.5
	v_lshlrev_b64 v[130:131], 11, v[130:131]
	v_cvt_pk_u8_f32 v135, v135, 0, 0
	v_fma_f32 v137, v140, s87, -0.5
	v_lshl_add_u64 v[130:131], s[22:23], 0, v[130:131]
	v_cvt_pk_u8_f32 v135, v137, 1, v135
	v_fma_f32 v137, v141, s87, -0.5
	v_lshl_add_u64 v[130:131], v[130:131], 0, s[24:25]
	v_cvt_pk_u8_f32 v135, v137, 2, v135
	v_fma_f32 v137, v142, s87, -0.5
	v_cvt_pk_u8_f32 v137, v137, 3, v135
	v_lshl_add_u64 v[138:139], v[130:131], 0, v[0:1]
	global_store_dwordx2 v[138:139], v[136:137], off
	v_mul_f32_e32 v0, 0xbd38aa3b, v6
	v_exp_f32_e32 v0, v0
	v_mul_f32_e32 v138, 0xbd38aa3b, v7
	v_exp_f32_e32 v138, v138
	v_mul_f32_e32 v136, 0xbd38aa3b, v8
	v_exp_f32_e32 v136, v136
	v_mul_f32_e32 v137, 0xbd38aa3b, v9
	v_mul_f32_e32 v135, 0xbd38aa3b, v2
	v_exp_f32_e32 v137, v137
	v_exp_f32_e32 v135, v135
	v_add_f32_e32 v0, 1.0, v0
	v_mul_f32_e32 v139, 0xbd38aa3b, v3
	v_rcp_f32_e32 v0, v0
	v_exp_f32_e32 v139, v139
	v_add_f32_e32 v138, 1.0, v138
	v_mul_f32_e32 v140, 0xbd38aa3b, v4
	v_rcp_f32_e32 v138, v138
	v_exp_f32_e32 v140, v140
	v_add_f32_e32 v136, 1.0, v136
	v_mul_f32_e32 v141, 0xbd38aa3b, v5
	v_rcp_f32_e32 v136, v136
	v_exp_f32_e32 v141, v141
	v_add_f32_e32 v137, 1.0, v137
	v_add_f32_e32 v135, 1.0, v135
	v_rcp_f32_e32 v137, v137
	v_rcp_f32_e32 v135, v135
	v_add_f32_e32 v139, 1.0, v139
	v_fma_f32 v0, v0, s87, -0.5
	v_rcp_f32_e32 v139, v139
	v_add_f32_e32 v140, 1.0, v140
	v_cvt_pk_u8_f32 v0, v0, 0, 0
	v_fma_f32 v138, v138, s87, -0.5
	v_rcp_f32_e32 v140, v140
	v_add_f32_e32 v141, 1.0, v141
	v_cvt_pk_u8_f32 v0, v138, 1, v0
	v_fma_f32 v136, v136, s87, -0.5
	v_rcp_f32_e32 v141, v141
	v_cvt_pk_u8_f32 v0, v136, 2, v0
	v_fma_f32 v136, v137, s87, -0.5
	v_cvt_pk_u8_f32 v136, v136, 3, v0
	v_fma_f32 v0, v135, s87, -0.5
	v_cvt_pk_u8_f32 v0, v0, 0, 0
	v_fma_f32 v135, v139, s87, -0.5
	v_cvt_pk_u8_f32 v0, v135, 1, v0
	v_fma_f32 v135, v140, s87, -0.5
	v_cvt_pk_u8_f32 v0, v135, 2, v0
	v_fma_f32 v135, v141, s87, -0.5
	v_cvt_pk_u8_f32 v137, v135, 3, v0
	v_lshl_add_u64 v[130:131], v[130:131], 0, v[132:133]
	global_store_dwordx2 v[130:131], v[136:137], off
	s_mov_b64 s[22:23], 0
